# idle workgroups of the layer-1 MoE down-projection GEMM tail round (runtime-sized) also convert weights (832 blocks); layer-2 w_out/FFN1 tails lightened to 1 block per CU
# speedup vs baseline: 1.0032x; 1.0003x over previous
.LBB0_109:
	v_readlane_b32 s0, v251, 5
	v_readlane_b32 s6, v251, 11
	v_readlane_b32 s7, v251, 12
	s_add_u32 s0, s6, 0x10f00000
	v_writelane_b32 v252, s0, 12
	s_addc_u32 s0, s7, 0
	v_writelane_b32 v252, s0, 13
	s_add_u32 s0, s6, 0x3c90c0
	v_writelane_b32 v252, s0, 14
	s_addc_u32 s0, s7, 0
	v_writelane_b32 v252, s0, 15
	s_add_u32 s0, s6, 0x3ad0c0
	v_writelane_b32 v252, s0, 16
	s_addc_u32 s0, s7, 0
	v_writelane_b32 v252, s0, 17
	s_add_u32 s0, s6, 0x13800000
	v_writelane_b32 v252, s0, 18
	s_addc_u32 s0, s7, 0
	v_writelane_b32 v252, s0, 19
	s_add_u32 s0, s6, 0x33d0c0
	v_writelane_b32 v252, s0, 20
	s_addc_u32 s0, s7, 0
	v_writelane_b32 v252, s0, 21
	s_add_u32 s0, s6, 0x11700000
	v_writelane_b32 v252, s0, 22
	s_addc_u32 s0, s7, 0
	v_writelane_b32 v252, s0, 23
	s_add_u32 s0, s6, 0x3320c0
	v_mov_b32_e32 v0, 0x135f
	v_readlane_b32 s1, v251, 6
	v_writelane_b32 v252, s0, 24
	s_addc_u32 s0, s7, 0
	v_cmp_gt_i32_e32 vcc, s28, v0
	v_readlane_b32 s2, v251, 7
	v_readlane_b32 s3, v251, 8
	v_readlane_b32 s4, v251, 9
	v_readlane_b32 s5, v251, 10
	v_writelane_b32 v252, s0, 25
	s_and_b64 s[0:1], vcc, exec
	s_mov_b64 s[0:1], s[52:53]
	s_mov_b64 s[2:3], s[54:55]
	s_mov_b64 s[4:5], s[56:57]
	s_mov_b64 s[6:7], s[58:59]
	s_mov_b64 s[8:9], s[60:61]
	s_mov_b64 s[10:11], s[62:63]
	s_mov_b64 s[12:13], s[64:65]
	v_writelane_b32 v252, s0, 26
	s_waitcnt lgkmcnt(0)
	s_barrier
	v_writelane_b32 v252, s1, 27
	v_writelane_b32 v252, s2, 28
	v_writelane_b32 v252, s3, 29
	v_writelane_b32 v252, s4, 30
	v_writelane_b32 v252, s5, 31
	v_writelane_b32 v252, s6, 32
	v_writelane_b32 v252, s7, 33
	v_writelane_b32 v252, s8, 34
	v_writelane_b32 v252, s9, 35
	v_writelane_b32 v252, s10, 36
	v_writelane_b32 v252, s11, 37
	v_writelane_b32 v252, s12, 38
	v_writelane_b32 v252, s13, 39
	v_writelane_b32 v252, s14, 40
	v_writelane_b32 v252, s15, 41
	s_cbranch_scc1 .LBB0_253
	s_mov_b32 s98, s28
	v_readlane_b32 s100, v251, 24
	s_movk_i32 s99, 0xe0
	s_mov_b32 s101, 0
	s_mov_b32 s0, 0xfffffc00
	s_cmp_lt_u32 s98, 0x1278
	s_cselect_b32 s0, 0xfffffc00, s0
	s_cmp_lt_u32 s98, 0x11d0
	s_cselect_b32 s0, 0xfffffc00, s0
	s_cmp_lt_u32 s98, 0x10e0
	s_cselect_b32 s0, 0xfffffc00, s0
	s_cmp_lt_u32 s98, 0xf40
	s_cselect_b32 s0, 0xfffffc00, s0
	s_cmp_lt_u32 s98, 0xc60
	s_cselect_b32 s0, 0x700, s0
	s_cmp_lt_u32 s98, 0xc40
	s_cselect_b32 s0, 0x6a0, s0
	s_cmp_lt_u32 s98, 0xc00
	s_cselect_b32 s0, 0x6a0, s0
	s_cmp_lt_u32 s98, 0xb60
	s_cselect_b32 s0, 0xfffff600, s0
	s_cmp_lt_u32 s98, 0xab0
	s_cselect_b32 s0, 0x890, s0
	s_cmp_lt_u32 s98, 0xa90
	s_cselect_b32 s0, 0x770, s0
	s_cmp_lt_u32 s98, 0xa20
	s_cselect_b32 s0, 0x770, s0
	s_cmp_lt_u32 s98, 0x9b0
	s_cselect_b32 s0, 0xfffffeb0, s0
	s_cmp_lt_u32 s98, 0x880
	s_cselect_b32 s0, 0xfffffeb0, s0
	s_cmp_lt_u32 s98, 0x5b0
	s_cselect_b32 s0, 0xfffffeb0, s0
	s_cmp_lt_u32 s98, 0x460
	s_cselect_b32 s0, 0xfffffeb0, s0
	s_cmp_lt_u32 s98, 0x2b0
	s_cselect_b32 s0, 0x1070, s0
	s_cmp_lt_u32 s98, 0x290
	s_cselect_b32 s0, 0xe90, s0
	s_cmp_lt_u32 s98, 0x280
	s_cselect_b32 s0, 0xe90, s0
	s_cmp_lt_u32 s98, 0x1b0
	s_cselect_b32 s0, 0xffffff00, s0
	s_cmp_lt_u32 s98, 0x100
	s_cselect_b32 s0, 0x1200, s0
	s_cmp_lt_u32 s98, 0xe0
	s_cselect_b32 s0, 0xf60, s0
	s_add_i32 s28, s98, s0
	v_lshlrev_b32_e32 v0, 2, v50
	s_add_i32 s0, 0, 0x21000
	v_and_b32_e32 v37, 31, v50
	v_add_u32_e32 v39, s0, v0
	v_cmp_gt_i32_e64 s[0:1], 32, v50
	v_lshlrev_b32_e32 v1, 1, v50
	v_lshlrev_b32_e32 v42, 2, v37
	v_writelane_b32 v252, s0, 42
	v_ashrrev_i32_e32 v40, 3, v50
	v_and_b32_e32 v2, 0xffffffc0, v1
	v_add_u32_e32 v4, 0, v42
	v_writelane_b32 v252, s1, 43
	s_add_i32 s0, 0, 0x21800
	s_movk_i32 s2, 0x84
	v_and_b32_e32 v45, 7, v50
	v_add_u32_e32 v43, s0, v0
	v_add_u32_e32 v82, s0, v42
	v_mad_u64_u32 v[6:7], s[0:1], v2, s2, v[4:5]
	v_mul_lo_u32 v41, v40, s2
	v_lshlrev_b32_e32 v45, 4, v45
	v_add3_u32 v83, v41, v45, 0
	v_lshrrev_b32_e32 v45, 5, v50
	s_movk_i32 s0, 0x2100
	v_and_b32_e32 v35, 28, v0
	v_or_b32_e32 v0, 62, v1
	v_or_b32_e32 v1, 63, v1
	v_mul_lo_u32 v84, v45, s0
	v_mul_lo_u32 v0, v0, s2
	v_mul_lo_u32 v44, v1, s2
	v_or_b32_e32 v10, 2, v2
	v_or_b32_e32 v12, 4, v2
	v_or_b32_e32 v14, 6, v2
	v_or_b32_e32 v16, 8, v2
	v_or_b32_e32 v18, 10, v2
	v_or_b32_e32 v20, 12, v2
	v_or_b32_e32 v22, 14, v2
	v_or_b32_e32 v24, 16, v2
	v_or_b32_e32 v26, 18, v2
	v_or_b32_e32 v28, 20, v2
	v_or_b32_e32 v30, 22, v2
	v_or_b32_e32 v32, 24, v2
	v_or_b32_e32 v34, 26, v2
	v_or_b32_e32 v36, 28, v2
	v_or_b32_e32 v38, 30, v2
	v_ashrrev_i32_e32 v41, 31, v40
	v_or_b32_e32 v42, v84, v42
	v_ashrrev_i32_e32 v3, 31, v2
	v_mov_b32_e32 v8, v2
	v_mov_b32_e32 v1, v2
	v_mov_b32_e32 v5, v10
	v_mov_b32_e32 v7, v12
	v_mov_b32_e32 v9, v14
	v_mov_b32_e32 v11, v16
	v_mov_b32_e32 v13, v18
	v_mov_b32_e32 v15, v20
	v_mov_b32_e32 v17, v22
	v_mov_b32_e32 v19, v24
	v_mov_b32_e32 v21, v26
	v_mov_b32_e32 v23, v28
	v_mov_b32_e32 v25, v30
	v_mov_b32_e32 v27, v32
	v_mov_b32_e32 v29, v34
	v_mov_b32_e32 v31, v36
	v_mov_b32_e32 v33, v38
	v_lshlrev_b64 v[40:41], 2, v[40:41]
	v_add_u32_e32 v42, 0, v42
	v_mov_b32_e32 v45, 0
	v_add_u32_e32 v85, v4, v0
	v_add_u32_e32 v86, v4, v44
	s_branch .LBB0_112
.LBB0_111:
	s_or_b64 exec, exec, s[0:1]
	s_waitcnt lgkmcnt(0)
	s_barrier
	ds_read_b32 v0, v82
	ds_read_b32 v44, v85
	ds_read_b32 v58, v86
	s_mov_b32 s2, 0x42fe0000
	v_add_u32_e32 v57, 0x400, v6
	s_waitcnt lgkmcnt(2)
	v_div_scale_f32 v46, s[0:1], v0, v0, s2
	v_rcp_f32_e32 v47, v46
	v_readlane_b32 s0, v252, 46
	v_readlane_b32 s1, v252, 47
	v_add_u32_e32 v60, 0x800, v6
	v_fma_f32 v48, -v46, v47, 1.0
	v_fmac_f32_e32 v47, v48, v47
	v_div_scale_f32 v48, vcc, s2, v0, s2
	v_mul_f32_e32 v49, v48, v47
	v_fma_f32 v52, -v46, v49, v48
	v_fmac_f32_e32 v49, v52, v47
	v_fma_f32 v46, -v46, v49, v48
	v_div_fmas_f32 v46, v46, v47, v49
	ds_read2_b32 v[48:49], v6 offset1:33
	v_div_fixup_f32 v46, v46, v0, s2
	v_cmp_lt_f32_e32 vcc, 0, v0
	ds_read2_b32 v[52:53], v6 offset0:66 offset1:99
	v_readlane_b32 s28, v252, 44
	v_cndmask_b32_e32 v0, 0, v46, vcc
	s_waitcnt lgkmcnt(1)
	v_mul_f32_e32 v48, v48, v0
	v_rndne_f32_e32 v48, v48
	v_cvt_i32_f32_e32 v54, v48
	v_mul_f32_e32 v48, v0, v49
	v_rndne_f32_e32 v48, v48
	v_cvt_i32_f32_e32 v55, v48
	s_waitcnt lgkmcnt(0)
	v_mul_f32_e32 v48, v0, v52
	v_rndne_f32_e32 v48, v48
	v_cvt_i32_f32_sdwa v52, v48 dst_sel:WORD_1 dst_unused:UNUSED_PAD src0_sel:DWORD
	v_mul_f32_e32 v48, v0, v53
	v_or_b32_e32 v46, s33, v37
	v_rndne_f32_e32 v48, v48
	v_ashrrev_i32_e32 v47, 31, v46
	v_cvt_i32_f32_sdwa v53, v48 dst_sel:BYTE_3 dst_unused:UNUSED_PAD src0_sel:DWORD
	ds_read2_b32 v[48:49], v6 offset0:132 offset1:165
	v_lshlrev_b64 v[46:47], 10, v[46:47]
	v_lshl_add_u64 v[46:47], s[0:1], 0, v[46:47]
	v_lshlrev_b32_e32 v55, 8, v55
	s_mov_b32 s0, 0xc0c0500
	v_perm_b32 v54, v55, v54, s0
	v_and_b32_e32 v52, 0xff0000, v52
	v_or3_b32 v52, v54, v52, v53
	ds_read2_b32 v[54:55], v6 offset0:198 offset1:231
	s_waitcnt lgkmcnt(1)
	v_mul_f32_e32 v48, v0, v48
	v_rndne_f32_e32 v48, v48
	v_cvt_i32_f32_e32 v53, v48
	v_mul_f32_e32 v48, v0, v49
	v_rndne_f32_e32 v48, v48
	v_cvt_i32_f32_e32 v56, v48
	s_waitcnt lgkmcnt(0)
	v_mul_f32_e32 v48, v0, v54
	v_rndne_f32_e32 v48, v48
	v_cvt_i32_f32_sdwa v54, v48 dst_sel:WORD_1 dst_unused:UNUSED_PAD src0_sel:DWORD
	v_mul_f32_e32 v48, v0, v55
	v_rndne_f32_e32 v48, v48
	v_cvt_i32_f32_sdwa v55, v48 dst_sel:BYTE_3 dst_unused:UNUSED_PAD src0_sel:DWORD
	ds_read2_b32 v[48:49], v57 offset0:8 offset1:41
	v_lshlrev_b32_e32 v56, 8, v56
	v_perm_b32 v53, v56, v53, s0
	v_and_b32_e32 v54, 0xff0000, v54
	v_or3_b32 v53, v53, v54, v55
	ds_read2_b32 v[54:55], v57 offset0:74 offset1:107
	s_waitcnt lgkmcnt(1)
	v_mul_f32_e32 v48, v0, v48
	v_rndne_f32_e32 v48, v48
	v_cvt_i32_f32_e32 v56, v48
	v_mul_f32_e32 v48, v0, v49
	v_rndne_f32_e32 v48, v48
	v_cvt_i32_f32_e32 v59, v48
	s_waitcnt lgkmcnt(0)
	v_mul_f32_e32 v48, v0, v54
	v_rndne_f32_e32 v48, v48
	v_cvt_i32_f32_sdwa v54, v48 dst_sel:WORD_1 dst_unused:UNUSED_PAD src0_sel:DWORD
	v_mul_f32_e32 v48, v0, v55
	v_rndne_f32_e32 v48, v48
	v_cvt_i32_f32_sdwa v55, v48 dst_sel:BYTE_3 dst_unused:UNUSED_PAD src0_sel:DWORD
	ds_read2_b32 v[48:49], v57 offset0:140 offset1:173
	v_lshlrev_b32_e32 v59, 8, v59
	v_perm_b32 v56, v59, v56, s0
	v_and_b32_e32 v54, 0xff0000, v54
	v_or3_b32 v54, v56, v54, v55
	ds_read2_b32 v[56:57], v57 offset0:206 offset1:239
	s_waitcnt lgkmcnt(1)
	v_mul_f32_e32 v48, v0, v48
	v_mul_f32_e32 v49, v0, v49
	v_rndne_f32_e32 v48, v48
	v_rndne_f32_e32 v49, v49
	v_cvt_i32_f32_e32 v55, v48
	s_waitcnt lgkmcnt(0)
	v_mul_f32_e32 v48, v0, v56
	v_cvt_i32_f32_e32 v49, v49
	v_rndne_f32_e32 v48, v48
	v_cvt_i32_f32_sdwa v56, v48 dst_sel:WORD_1 dst_unused:UNUSED_PAD src0_sel:DWORD
	v_mul_f32_e32 v48, v0, v57
	v_rndne_f32_e32 v48, v48
	v_cvt_i32_f32_sdwa v57, v48 dst_sel:BYTE_3 dst_unused:UNUSED_PAD src0_sel:DWORD
	v_lshlrev_b32_e32 v59, 8, v49
	ds_read2_b32 v[48:49], v60 offset0:16 offset1:49
	v_perm_b32 v55, v59, v55, s0
	v_and_b32_e32 v56, 0xff0000, v56
	v_lshl_add_u64 v[46:47], v[46:47], 0, v[2:3]
	v_or3_b32 v55, v55, v56, v57
	global_store_dwordx4 v[46:47], v[52:55], off
	ds_read2_b32 v[52:53], v60 offset0:82 offset1:115
	s_waitcnt lgkmcnt(1)
	v_mul_f32_e32 v48, v0, v48
	v_rndne_f32_e32 v48, v48
	v_cvt_i32_f32_e32 v54, v48
	v_mul_f32_e32 v48, v0, v49
	v_rndne_f32_e32 v48, v48
	v_cvt_i32_f32_e32 v55, v48
	s_waitcnt lgkmcnt(0)
	v_mul_f32_e32 v48, v0, v52
	v_rndne_f32_e32 v48, v48
	v_cvt_i32_f32_sdwa v52, v48 dst_sel:WORD_1 dst_unused:UNUSED_PAD src0_sel:DWORD
	v_mul_f32_e32 v48, v0, v53
	v_rndne_f32_e32 v48, v48
	v_cvt_i32_f32_sdwa v53, v48 dst_sel:BYTE_3 dst_unused:UNUSED_PAD src0_sel:DWORD
	ds_read2_b32 v[48:49], v60 offset0:148 offset1:181
	v_lshlrev_b32_e32 v55, 8, v55
	v_perm_b32 v54, v55, v54, s0
	v_and_b32_e32 v52, 0xff0000, v52
	v_or3_b32 v52, v54, v52, v53
	ds_read2_b32 v[54:55], v60 offset0:214 offset1:247
	s_waitcnt lgkmcnt(1)
	v_mul_f32_e32 v48, v0, v48
	v_rndne_f32_e32 v48, v48
	v_cvt_i32_f32_e32 v53, v48
	v_mul_f32_e32 v48, v0, v49
	v_rndne_f32_e32 v48, v48
	v_cvt_i32_f32_e32 v56, v48
	s_waitcnt lgkmcnt(0)
	v_mul_f32_e32 v48, v0, v54
	v_rndne_f32_e32 v48, v48
	v_cvt_i32_f32_sdwa v54, v48 dst_sel:WORD_1 dst_unused:UNUSED_PAD src0_sel:DWORD
	v_mul_f32_e32 v48, v0, v55
	v_rndne_f32_e32 v48, v48
	v_add_u32_e32 v57, 0xc00, v6
	v_cvt_i32_f32_sdwa v55, v48 dst_sel:BYTE_3 dst_unused:UNUSED_PAD src0_sel:DWORD
	ds_read2_b32 v[48:49], v57 offset0:24 offset1:57
	v_lshlrev_b32_e32 v56, 8, v56
	v_perm_b32 v53, v56, v53, s0
	v_and_b32_e32 v54, 0xff0000, v54
	v_or3_b32 v53, v53, v54, v55
	ds_read2_b32 v[54:55], v57 offset0:90 offset1:123
	s_waitcnt lgkmcnt(1)
	v_mul_f32_e32 v48, v0, v48
	v_rndne_f32_e32 v48, v48
	v_cvt_i32_f32_e32 v56, v48
	v_mul_f32_e32 v48, v0, v49
	v_rndne_f32_e32 v48, v48
	v_cvt_i32_f32_e32 v59, v48
	s_waitcnt lgkmcnt(0)
	v_mul_f32_e32 v48, v0, v54
	v_rndne_f32_e32 v48, v48
	v_cvt_i32_f32_sdwa v54, v48 dst_sel:WORD_1 dst_unused:UNUSED_PAD src0_sel:DWORD
	v_mul_f32_e32 v48, v0, v55
	v_rndne_f32_e32 v48, v48
	v_cvt_i32_f32_sdwa v55, v48 dst_sel:BYTE_3 dst_unused:UNUSED_PAD src0_sel:DWORD
	ds_read2_b32 v[48:49], v57 offset0:156 offset1:189
	v_lshlrev_b32_e32 v59, 8, v59
	v_perm_b32 v56, v59, v56, s0
	v_and_b32_e32 v54, 0xff0000, v54
	v_or3_b32 v54, v56, v54, v55
	ds_read2_b32 v[56:57], v57 offset0:222 offset1:255
	s_waitcnt lgkmcnt(1)
	v_mul_f32_e32 v48, v0, v48
	v_mul_f32_e32 v49, v0, v49
	v_rndne_f32_e32 v48, v48
	v_rndne_f32_e32 v49, v49
	v_cvt_i32_f32_e32 v55, v48
	s_waitcnt lgkmcnt(0)
	v_mul_f32_e32 v48, v0, v56
	v_cvt_i32_f32_e32 v49, v49
	v_rndne_f32_e32 v48, v48
	v_cvt_i32_f32_sdwa v56, v48 dst_sel:WORD_1 dst_unused:UNUSED_PAD src0_sel:DWORD
	v_mul_f32_e32 v48, v0, v57
	v_rndne_f32_e32 v48, v48
	v_cvt_i32_f32_sdwa v57, v48 dst_sel:BYTE_3 dst_unused:UNUSED_PAD src0_sel:DWORD
	v_add_u32_e32 v60, 0x1000, v6
	v_lshlrev_b32_e32 v59, 8, v49
	ds_read2_b32 v[48:49], v60 offset0:32 offset1:65
	v_perm_b32 v55, v59, v55, s0
	v_and_b32_e32 v56, 0xff0000, v56
	v_or3_b32 v55, v55, v56, v57
	global_store_dwordx4 v[46:47], v[52:55], off offset:16
	ds_read2_b32 v[52:53], v60 offset0:98 offset1:131
	s_waitcnt lgkmcnt(1)
	v_mul_f32_e32 v48, v0, v48
	v_rndne_f32_e32 v48, v48
	v_cvt_i32_f32_e32 v54, v48
	v_mul_f32_e32 v48, v0, v49
	v_rndne_f32_e32 v48, v48
	v_cvt_i32_f32_e32 v55, v48
	s_waitcnt lgkmcnt(0)
	v_mul_f32_e32 v48, v0, v52
	v_rndne_f32_e32 v48, v48
	v_cvt_i32_f32_sdwa v52, v48 dst_sel:WORD_1 dst_unused:UNUSED_PAD src0_sel:DWORD
	v_mul_f32_e32 v48, v0, v53
	v_rndne_f32_e32 v48, v48
	v_cvt_i32_f32_sdwa v53, v48 dst_sel:BYTE_3 dst_unused:UNUSED_PAD src0_sel:DWORD
	ds_read2_b32 v[48:49], v60 offset0:164 offset1:197
	v_lshlrev_b32_e32 v55, 8, v55
	v_perm_b32 v54, v55, v54, s0
	v_and_b32_e32 v52, 0xff0000, v52
	v_or3_b32 v52, v54, v52, v53
	v_add_u32_e32 v53, 0x1200, v6
	ds_read2_b32 v[54:55], v53 offset0:102 offset1:135
	s_waitcnt lgkmcnt(1)
	v_mul_f32_e32 v48, v0, v48
	v_rndne_f32_e32 v48, v48
	v_cvt_i32_f32_e32 v53, v48
	v_mul_f32_e32 v48, v0, v49
	v_rndne_f32_e32 v48, v48
	v_cvt_i32_f32_e32 v56, v48
	s_waitcnt lgkmcnt(0)
	v_mul_f32_e32 v48, v0, v54
	v_rndne_f32_e32 v48, v48
	v_cvt_i32_f32_sdwa v54, v48 dst_sel:WORD_1 dst_unused:UNUSED_PAD src0_sel:DWORD
	v_mul_f32_e32 v48, v0, v55
	v_rndne_f32_e32 v48, v48
	v_add_u32_e32 v57, 0x1400, v6
	v_cvt_i32_f32_sdwa v55, v48 dst_sel:BYTE_3 dst_unused:UNUSED_PAD src0_sel:DWORD
	ds_read2_b32 v[48:49], v57 offset0:40 offset1:73
	v_lshlrev_b32_e32 v56, 8, v56
	v_perm_b32 v53, v56, v53, s0
	v_and_b32_e32 v54, 0xff0000, v54
	v_or3_b32 v53, v53, v54, v55
	ds_read2_b32 v[54:55], v57 offset0:106 offset1:139
	s_waitcnt lgkmcnt(1)
	v_mul_f32_e32 v48, v0, v48
	v_rndne_f32_e32 v48, v48
	v_cvt_i32_f32_e32 v56, v48
	v_mul_f32_e32 v48, v0, v49
	v_rndne_f32_e32 v48, v48
	v_cvt_i32_f32_e32 v59, v48
	s_waitcnt lgkmcnt(0)
	v_mul_f32_e32 v48, v0, v54
	v_rndne_f32_e32 v48, v48
	v_cvt_i32_f32_sdwa v54, v48 dst_sel:WORD_1 dst_unused:UNUSED_PAD src0_sel:DWORD
	v_mul_f32_e32 v48, v0, v55
	v_rndne_f32_e32 v48, v48
	v_cvt_i32_f32_sdwa v55, v48 dst_sel:BYTE_3 dst_unused:UNUSED_PAD src0_sel:DWORD
	ds_read2_b32 v[48:49], v57 offset0:172 offset1:205
	v_lshlrev_b32_e32 v57, 8, v59
	v_perm_b32 v56, v57, v56, s0
	v_and_b32_e32 v54, 0xff0000, v54
	v_or3_b32 v54, v56, v54, v55
	v_add_u32_e32 v55, 0x1600, v6
	ds_read2_b32 v[56:57], v55 offset0:110 offset1:143
	s_waitcnt lgkmcnt(1)
	v_mul_f32_e32 v48, v0, v48
	v_mul_f32_e32 v49, v0, v49
	v_rndne_f32_e32 v48, v48
	v_rndne_f32_e32 v49, v49
	v_cvt_i32_f32_e32 v55, v48
	s_waitcnt lgkmcnt(0)
	v_mul_f32_e32 v48, v0, v56
	v_cvt_i32_f32_e32 v49, v49
	v_rndne_f32_e32 v48, v48
	v_cvt_i32_f32_sdwa v56, v48 dst_sel:WORD_1 dst_unused:UNUSED_PAD src0_sel:DWORD
	v_mul_f32_e32 v48, v0, v57
	v_rndne_f32_e32 v48, v48
	v_cvt_i32_f32_sdwa v57, v48 dst_sel:BYTE_3 dst_unused:UNUSED_PAD src0_sel:DWORD
	v_add_u32_e32 v60, 0x1800, v6
	v_lshlrev_b32_e32 v59, 8, v49
	ds_read2_b32 v[48:49], v60 offset0:48 offset1:81
	v_perm_b32 v55, v59, v55, s0
	v_and_b32_e32 v56, 0xff0000, v56
	v_or3_b32 v55, v55, v56, v57
	global_store_dwordx4 v[46:47], v[52:55], off offset:32
	ds_read2_b32 v[52:53], v60 offset0:114 offset1:147
	s_waitcnt lgkmcnt(1)
	v_mul_f32_e32 v48, v0, v48
	v_rndne_f32_e32 v48, v48
	v_cvt_i32_f32_e32 v54, v48
	v_mul_f32_e32 v48, v0, v49
	v_rndne_f32_e32 v48, v48
	v_cvt_i32_f32_e32 v55, v48
	s_waitcnt lgkmcnt(0)
	v_mul_f32_e32 v48, v0, v52
	v_rndne_f32_e32 v48, v48
	v_cvt_i32_f32_sdwa v52, v48 dst_sel:WORD_1 dst_unused:UNUSED_PAD src0_sel:DWORD
	v_mul_f32_e32 v48, v0, v53
	v_rndne_f32_e32 v48, v48
	v_cvt_i32_f32_sdwa v53, v48 dst_sel:BYTE_3 dst_unused:UNUSED_PAD src0_sel:DWORD
	ds_read2_b32 v[48:49], v60 offset0:180 offset1:213
	v_lshlrev_b32_e32 v55, 8, v55
	v_perm_b32 v54, v55, v54, s0
	v_and_b32_e32 v52, 0xff0000, v52
	v_or3_b32 v52, v54, v52, v53
	v_add_u32_e32 v53, 0x1a00, v6
	ds_read2_b32 v[54:55], v53 offset0:118 offset1:151
	s_waitcnt lgkmcnt(1)
	v_mul_f32_e32 v48, v0, v48
	v_rndne_f32_e32 v48, v48
	v_cvt_i32_f32_e32 v53, v48
	v_mul_f32_e32 v48, v0, v49
	v_rndne_f32_e32 v48, v48
	v_cvt_i32_f32_e32 v56, v48
	s_waitcnt lgkmcnt(0)
	v_mul_f32_e32 v48, v0, v54
	v_rndne_f32_e32 v48, v48
	v_cvt_i32_f32_sdwa v54, v48 dst_sel:WORD_1 dst_unused:UNUSED_PAD src0_sel:DWORD
	v_mul_f32_e32 v48, v0, v55
	v_rndne_f32_e32 v48, v48
	v_add_u32_e32 v57, 0x1c00, v6
	v_cvt_i32_f32_sdwa v55, v48 dst_sel:BYTE_3 dst_unused:UNUSED_PAD src0_sel:DWORD
	ds_read2_b32 v[48:49], v57 offset0:56 offset1:89
	v_lshlrev_b32_e32 v56, 8, v56
	v_perm_b32 v53, v56, v53, s0
	v_and_b32_e32 v54, 0xff0000, v54
	v_or3_b32 v53, v53, v54, v55
	ds_read2_b32 v[54:55], v57 offset0:122 offset1:155
	s_waitcnt lgkmcnt(1)
	v_mul_f32_e32 v48, v0, v48
	v_rndne_f32_e32 v48, v48
	v_cvt_i32_f32_e32 v56, v48
	v_mul_f32_e32 v48, v0, v49
	v_rndne_f32_e32 v48, v48
	v_cvt_i32_f32_e32 v59, v48
	s_waitcnt lgkmcnt(0)
	v_mul_f32_e32 v48, v0, v54
	v_rndne_f32_e32 v48, v48
	v_cvt_i32_f32_sdwa v54, v48 dst_sel:WORD_1 dst_unused:UNUSED_PAD src0_sel:DWORD
	v_mul_f32_e32 v48, v0, v55
	v_rndne_f32_e32 v48, v48
	v_cvt_i32_f32_sdwa v55, v48 dst_sel:BYTE_3 dst_unused:UNUSED_PAD src0_sel:DWORD
	ds_read2_b32 v[48:49], v57 offset0:188 offset1:221
	v_mul_f32_e32 v44, v0, v44
	v_rndne_f32_e32 v44, v44
	v_cvt_i32_f32_sdwa v44, v44 dst_sel:WORD_1 dst_unused:UNUSED_PAD src0_sel:DWORD
	v_lshlrev_b32_e32 v57, 8, v59
	s_waitcnt lgkmcnt(0)
	v_mul_f32_e32 v49, v0, v49
	v_mul_f32_e32 v48, v0, v48
	v_rndne_f32_e32 v49, v49
	v_rndne_f32_e32 v48, v48
	v_cvt_i32_f32_e32 v49, v49
	v_cvt_i32_f32_e32 v48, v48
	v_mul_f32_e32 v0, v0, v58
	v_rndne_f32_e32 v0, v0
	v_cvt_i32_f32_sdwa v0, v0 dst_sel:BYTE_3 dst_unused:UNUSED_PAD src0_sel:DWORD
	v_lshlrev_b32_e32 v49, 8, v49
	v_perm_b32 v56, v57, v56, s0
	v_perm_b32 v48, v49, v48, s0
	s_add_i32 s98, s98, s100
	v_and_b32_e32 v54, 0xff0000, v54
	v_and_b32_e32 v44, 0xff0000, v44
	s_mov_b32 s0, 0xfffffc00
	s_cmp_lt_u32 s98, 0x1278
	s_cselect_b32 s0, 0xfffffc00, s0
	s_cmp_lt_u32 s98, 0x11d0
	s_cselect_b32 s0, 0xfffffc00, s0
	s_cmp_lt_u32 s98, 0x10e0
	s_cselect_b32 s0, 0xfffffc00, s0
	s_cmp_lt_u32 s98, 0xf40
	s_cselect_b32 s0, 0xfffffc00, s0
	s_cmp_lt_u32 s98, 0xc60
	s_cselect_b32 s0, 0x700, s0
	s_cmp_lt_u32 s98, 0xc40
	s_cselect_b32 s0, 0x6a0, s0
	s_cmp_lt_u32 s98, 0xc00
	s_cselect_b32 s0, 0x6a0, s0
	s_cmp_lt_u32 s98, 0xb60
	s_cselect_b32 s0, 0xfffff600, s0
	s_cmp_lt_u32 s98, 0xab0
	s_cselect_b32 s0, 0x890, s0
	s_cmp_lt_u32 s98, 0xa90
	s_cselect_b32 s0, 0x770, s0
	s_cmp_lt_u32 s98, 0xa20
	s_cselect_b32 s0, 0x770, s0
	s_cmp_lt_u32 s98, 0x9b0
	s_cselect_b32 s0, 0xfffffeb0, s0
	s_cmp_lt_u32 s98, 0x880
	s_cselect_b32 s0, 0xfffffeb0, s0
	s_cmp_lt_u32 s98, 0x5b0
	s_cselect_b32 s0, 0xfffffeb0, s0
	s_cmp_lt_u32 s98, 0x460
	s_cselect_b32 s0, 0xfffffeb0, s0
	s_cmp_lt_u32 s98, 0x2b0
	s_cselect_b32 s0, 0x1070, s0
	s_cmp_lt_u32 s98, 0x290
	s_cselect_b32 s0, 0xe90, s0
	s_cmp_lt_u32 s98, 0x280
	s_cselect_b32 s0, 0xe90, s0
	s_cmp_lt_u32 s98, 0x1b0
	s_cselect_b32 s0, 0xffffff00, s0
	s_cmp_lt_u32 s98, 0x100
	s_cselect_b32 s0, 0x1200, s0
	s_cmp_lt_u32 s98, 0xe0
	s_cselect_b32 s0, 0xf60, s0
	s_add_i32 s28, s98, s0
	v_or3_b32 v54, v56, v54, v55
	v_or3_b32 v55, v48, v44, v0
	s_cmp_ge_u32 s98, s99
	global_store_dwordx4 v[46:47], v[52:55], off offset:48
	s_barrier
	s_cbranch_scc1 .LBB0_253

.LBB0_1028:
	v_readlane_b32 s98, v251, 3
	v_readlane_b32 s99, v255, 29
	s_cmp_lt_u32 s98, 48
	s_cbranch_scc1 .Lwqd_skip_M
	s_sub_i32 s98, s98, 48
	s_mov_b32 s100, 0
	s_mov_b32 s101, 0
	s_cmp_eq_u32 s99, 0
	s_cselect_b32 s100, 0xe0, s100
	s_cselect_b32 s101, 0x280, s101
	s_cmp_eq_u32 s99, 1
	s_cselect_b32 s100, 0x880, s100
	s_cselect_b32 s101, 0xa20, s101
	s_cmp_eq_u32 s99, 2
	s_cselect_b32 s100, 0xf40, s100
	s_cselect_b32 s101, 0x10e0, s101
	s_add_i32 s98, s98, s100
	s_mov_b32 s99, s101
	s_cmp_ge_u32 s98, s99
	s_cbranch_scc1 .Lwqd_skip_M
	s_movk_i32 s100, 208
	s_mov_b32 s101, 3
	v_writelane_b32 v117, s0, 0
	v_writelane_b32 v117, s1, 1
	v_writelane_b32 v117, s2, 2
	v_writelane_b32 v117, s3, 3
	v_writelane_b32 v117, s4, 4
	v_writelane_b32 v117, s5, 5
	v_writelane_b32 v117, s6, 6
	v_writelane_b32 v117, s7, 7
	v_writelane_b32 v117, s8, 8
	v_writelane_b32 v117, s9, 9
	v_writelane_b32 v117, s10, 10
	v_writelane_b32 v117, s11, 11
	v_writelane_b32 v117, s12, 12
	v_writelane_b32 v117, s13, 13
	v_writelane_b32 v117, s14, 14
	v_writelane_b32 v117, s15, 15
	v_writelane_b32 v117, s16, 16
	v_writelane_b32 v117, s17, 17
	v_writelane_b32 v117, s18, 18
	v_writelane_b32 v117, s19, 19
	v_writelane_b32 v117, s20, 20
	v_writelane_b32 v117, s21, 21
	v_writelane_b32 v117, s22, 22
	v_writelane_b32 v117, s23, 23
	v_writelane_b32 v117, s24, 24
	v_writelane_b32 v117, s25, 25
	v_writelane_b32 v117, s26, 26
	v_writelane_b32 v117, s27, 27
	v_writelane_b32 v117, s28, 28
	v_writelane_b32 v117, s29, 29
	v_writelane_b32 v117, s30, 30
	v_writelane_b32 v117, s31, 31
	v_writelane_b32 v117, s32, 32
	v_writelane_b32 v117, s33, 33
	v_writelane_b32 v117, s34, 34
	v_writelane_b32 v117, s35, 35
	v_writelane_b32 v117, s36, 36
	v_writelane_b32 v117, s37, 37
	v_writelane_b32 v117, s38, 38
	v_writelane_b32 v117, s39, 39
	v_writelane_b32 v117, s40, 40
	v_writelane_b32 v117, s41, 41
	v_writelane_b32 v117, s42, 42
	v_writelane_b32 v117, s43, 43
	v_writelane_b32 v117, s44, 44
	v_writelane_b32 v117, s45, 45
	v_writelane_b32 v117, s46, 46
	v_writelane_b32 v117, s47, 47
	v_writelane_b32 v117, s48, 48
	v_writelane_b32 v117, s49, 49
	v_writelane_b32 v117, s50, 50
	v_writelane_b32 v117, s51, 51
	v_writelane_b32 v117, s52, 52
	v_writelane_b32 v117, s53, 53
	v_writelane_b32 v117, s54, 54
	v_writelane_b32 v117, s55, 55
	v_writelane_b32 v117, s56, 56
	v_writelane_b32 v117, s57, 57
	v_writelane_b32 v117, s58, 58
	v_writelane_b32 v117, s59, 59
	v_writelane_b32 v117, s60, 60
	v_writelane_b32 v117, s61, 61
	v_writelane_b32 v117, s62, 62
	v_writelane_b32 v117, s63, 63
	v_writelane_b32 v118, s64, 0
	v_writelane_b32 v118, s65, 1
	v_writelane_b32 v118, s66, 2
	v_writelane_b32 v118, s67, 3
	v_writelane_b32 v118, s68, 4
	v_writelane_b32 v118, s69, 5
	v_writelane_b32 v118, s70, 6
	v_writelane_b32 v118, s71, 7
	v_writelane_b32 v118, s72, 8
	v_writelane_b32 v118, s73, 9
	v_writelane_b32 v118, s74, 10
	v_writelane_b32 v118, s75, 11
	v_writelane_b32 v118, s76, 12
	v_writelane_b32 v118, s77, 13
	v_writelane_b32 v118, s78, 14
	v_writelane_b32 v118, s79, 15
	v_writelane_b32 v118, s80, 16
	v_writelane_b32 v118, s81, 17
	v_writelane_b32 v118, s82, 18
	v_writelane_b32 v118, s83, 19
	v_writelane_b32 v118, s84, 20
	v_writelane_b32 v118, s85, 21
	v_writelane_b32 v118, s86, 22
	v_writelane_b32 v118, s87, 23
	v_writelane_b32 v118, s88, 24
	v_writelane_b32 v118, s89, 25
	v_writelane_b32 v118, s90, 26
	v_writelane_b32 v118, s91, 27
	v_writelane_b32 v118, s92, 28
	v_writelane_b32 v118, s93, 29
	v_writelane_b32 v118, s94, 30
	v_writelane_b32 v118, s95, 31
	v_writelane_b32 v118, s96, 32
	v_writelane_b32 v118, s97, 33
	v_mov_b32_e32 v100, v0
	v_mov_b32_e32 v101, v50
	v_mov_b32_e32 v102, v51
	v_mov_b32_e32 v103, v52
	v_mov_b32_e32 v104, v54
	v_mov_b32_e32 v105, v55
	v_mov_b32_e32 v106, v56
	v_mov_b32_e32 v107, v58
	v_mov_b32_e32 v108, v59
	v_mov_b32_e32 v109, v60
	v_mov_b32_e32 v110, v62
	v_mov_b32_e32 v111, v63
	v_mov_b32_e32 v112, v64
	v_mov_b32_e32 v113, v67
	v_mov_b32_e32 v114, v75
	v_mov_b32_e32 v115, v77
	s_branch .Lwqd_entry

.Lwqd_entry:
	v_mov_b32_e32 v50, v246
	v_mov_b32_e32 v5, 0
	v_readlane_b32 s52, v252, 26
	v_readlane_b32 s53, v252, 27
	s_mov_b32 s0, 0xfffffc00
	s_cmp_lt_u32 s98, 0x1278
	s_cselect_b32 s0, 0xfffffc00, s0
	s_cmp_lt_u32 s98, 0x11d0
	s_cselect_b32 s0, 0xfffffc00, s0
	s_cmp_lt_u32 s98, 0x10e0
	s_cselect_b32 s0, 0xfffffc00, s0
	s_cmp_lt_u32 s98, 0xf40
	s_cselect_b32 s0, 0xfffffc00, s0
	s_cmp_lt_u32 s98, 0xc60
	s_cselect_b32 s0, 0x700, s0
	s_cmp_lt_u32 s98, 0xc40
	s_cselect_b32 s0, 0x6a0, s0
	s_cmp_lt_u32 s98, 0xc00
	s_cselect_b32 s0, 0x6a0, s0
	s_cmp_lt_u32 s98, 0xb60
	s_cselect_b32 s0, 0xfffff600, s0
	s_cmp_lt_u32 s98, 0xab0
	s_cselect_b32 s0, 0x890, s0
	s_cmp_lt_u32 s98, 0xa90
	s_cselect_b32 s0, 0x770, s0
	s_cmp_lt_u32 s98, 0xa20
	s_cselect_b32 s0, 0x770, s0
	s_cmp_lt_u32 s98, 0x9b0
	s_cselect_b32 s0, 0xfffffeb0, s0
	s_cmp_lt_u32 s98, 0x880
	s_cselect_b32 s0, 0xfffffeb0, s0
	s_cmp_lt_u32 s98, 0x5b0
	s_cselect_b32 s0, 0xfffffeb0, s0
	s_cmp_lt_u32 s98, 0x460
	s_cselect_b32 s0, 0xfffffeb0, s0
	s_cmp_lt_u32 s98, 0x2b0
	s_cselect_b32 s0, 0x1070, s0
	s_cmp_lt_u32 s98, 0x290
	s_cselect_b32 s0, 0xe90, s0
	s_cmp_lt_u32 s98, 0x280
	s_cselect_b32 s0, 0xe90, s0
	s_cmp_lt_u32 s98, 0x1b0
	s_cselect_b32 s0, 0xffffff00, s0
	s_cmp_lt_u32 s98, 0x100
	s_cselect_b32 s0, 0x1200, s0
	s_cmp_lt_u32 s98, 0xe0
	s_cselect_b32 s0, 0xf60, s0
	s_add_i32 s28, s98, s0
	v_lshlrev_b32_e32 v0, 2, v50
	s_add_i32 s0, 0, 0x21000
	v_and_b32_e32 v37, 31, v50
	v_add_u32_e32 v39, s0, v0
	v_cmp_gt_i32_e64 s[0:1], 32, v50
	v_lshlrev_b32_e32 v1, 1, v50
	v_lshlrev_b32_e32 v42, 2, v37
	v_writelane_b32 v116, s0, 0
	v_ashrrev_i32_e32 v40, 3, v50
	v_and_b32_e32 v2, 0xffffffc0, v1
	v_add_u32_e32 v4, 0, v42
	v_writelane_b32 v116, s1, 1
	s_add_i32 s0, 0, 0x21800
	s_movk_i32 s2, 0x84
	v_and_b32_e32 v45, 7, v50
	v_add_u32_e32 v43, s0, v0
	v_add_u32_e32 v82, s0, v42
	v_mad_u64_u32 v[6:7], s[0:1], v2, s2, v[4:5]
	v_mul_lo_u32 v41, v40, s2
	v_lshlrev_b32_e32 v45, 4, v45
	v_add3_u32 v83, v41, v45, 0
	v_lshrrev_b32_e32 v45, 5, v50
	s_movk_i32 s0, 0x2100
	v_and_b32_e32 v35, 28, v0
	v_or_b32_e32 v0, 62, v1
	v_or_b32_e32 v1, 63, v1
	v_mul_lo_u32 v84, v45, s0
	v_mul_lo_u32 v0, v0, s2
	v_mul_lo_u32 v44, v1, s2
	v_or_b32_e32 v10, 2, v2
	v_or_b32_e32 v12, 4, v2
	v_or_b32_e32 v14, 6, v2
	v_or_b32_e32 v16, 8, v2
	v_or_b32_e32 v18, 10, v2
	v_or_b32_e32 v20, 12, v2
	v_or_b32_e32 v22, 14, v2
	v_or_b32_e32 v24, 16, v2
	v_or_b32_e32 v26, 18, v2
	v_or_b32_e32 v28, 20, v2
	v_or_b32_e32 v30, 22, v2
	v_or_b32_e32 v32, 24, v2
	v_or_b32_e32 v34, 26, v2
	v_or_b32_e32 v36, 28, v2
	v_or_b32_e32 v38, 30, v2
	v_ashrrev_i32_e32 v41, 31, v40
	v_or_b32_e32 v42, v84, v42
	v_ashrrev_i32_e32 v3, 31, v2
	v_mov_b32_e32 v8, v2
	v_mov_b32_e32 v1, v2
	v_mov_b32_e32 v5, v10
	v_mov_b32_e32 v7, v12
	v_mov_b32_e32 v9, v14
	v_mov_b32_e32 v11, v16
	v_mov_b32_e32 v13, v18
	v_mov_b32_e32 v15, v20
	v_mov_b32_e32 v17, v22
	v_mov_b32_e32 v19, v24
	v_mov_b32_e32 v21, v26
	v_mov_b32_e32 v23, v28
	v_mov_b32_e32 v25, v30
	v_mov_b32_e32 v27, v32
	v_mov_b32_e32 v29, v34
	v_mov_b32_e32 v31, v36
	v_mov_b32_e32 v33, v38
	v_lshlrev_b64 v[40:41], 2, v[40:41]
	v_add_u32_e32 v42, 0, v42
	v_mov_b32_e32 v45, 0
	v_add_u32_e32 v85, v4, v0
	v_add_u32_e32 v86, v4, v44
	s_branch .Lwqd_112
.Lwqd_111:
	s_or_b64 exec, exec, s[0:1]
	s_waitcnt lgkmcnt(0)
	s_barrier
	ds_read_b32 v0, v82
	ds_read_b32 v44, v85
	ds_read_b32 v58, v86
	s_mov_b32 s2, 0x42fe0000
	v_add_u32_e32 v57, 0x400, v6
	s_waitcnt lgkmcnt(2)
	v_div_scale_f32 v46, s[0:1], v0, v0, s2
	v_rcp_f32_e32 v47, v46
	v_readlane_b32 s0, v116, 4
	v_readlane_b32 s1, v116, 5
	v_add_u32_e32 v60, 0x800, v6
	v_fma_f32 v48, -v46, v47, 1.0
	v_fmac_f32_e32 v47, v48, v47
	v_div_scale_f32 v48, vcc, s2, v0, s2
	v_mul_f32_e32 v49, v48, v47
	v_fma_f32 v52, -v46, v49, v48
	v_fmac_f32_e32 v49, v52, v47
	v_fma_f32 v46, -v46, v49, v48
	v_div_fmas_f32 v46, v46, v47, v49
	ds_read2_b32 v[48:49], v6 offset1:33
	v_div_fixup_f32 v46, v46, v0, s2
	v_cmp_lt_f32_e32 vcc, 0, v0
	ds_read2_b32 v[52:53], v6 offset0:66 offset1:99
	v_readlane_b32 s28, v116, 2
	v_cndmask_b32_e32 v0, 0, v46, vcc
	s_waitcnt lgkmcnt(1)
	v_mul_f32_e32 v48, v48, v0
	v_rndne_f32_e32 v48, v48
	v_cvt_i32_f32_e32 v54, v48
	v_mul_f32_e32 v48, v0, v49
	v_rndne_f32_e32 v48, v48
	v_cvt_i32_f32_e32 v55, v48
	s_waitcnt lgkmcnt(0)
	v_mul_f32_e32 v48, v0, v52
	v_rndne_f32_e32 v48, v48
	v_cvt_i32_f32_sdwa v52, v48 dst_sel:WORD_1 dst_unused:UNUSED_PAD src0_sel:DWORD
	v_mul_f32_e32 v48, v0, v53
	v_or_b32_e32 v46, s33, v37
	v_rndne_f32_e32 v48, v48
	v_ashrrev_i32_e32 v47, 31, v46
	v_cvt_i32_f32_sdwa v53, v48 dst_sel:BYTE_3 dst_unused:UNUSED_PAD src0_sel:DWORD
	ds_read2_b32 v[48:49], v6 offset0:132 offset1:165
	v_lshlrev_b64 v[46:47], 10, v[46:47]
	v_lshl_add_u64 v[46:47], s[0:1], 0, v[46:47]
	v_lshlrev_b32_e32 v55, 8, v55
	s_mov_b32 s0, 0xc0c0500
	v_perm_b32 v54, v55, v54, s0
	v_and_b32_e32 v52, 0xff0000, v52
	v_or3_b32 v52, v54, v52, v53
	ds_read2_b32 v[54:55], v6 offset0:198 offset1:231
	s_waitcnt lgkmcnt(1)
	v_mul_f32_e32 v48, v0, v48
	v_rndne_f32_e32 v48, v48
	v_cvt_i32_f32_e32 v53, v48
	v_mul_f32_e32 v48, v0, v49
	v_rndne_f32_e32 v48, v48
	v_cvt_i32_f32_e32 v56, v48
	s_waitcnt lgkmcnt(0)
	v_mul_f32_e32 v48, v0, v54
	v_rndne_f32_e32 v48, v48
	v_cvt_i32_f32_sdwa v54, v48 dst_sel:WORD_1 dst_unused:UNUSED_PAD src0_sel:DWORD
	v_mul_f32_e32 v48, v0, v55
	v_rndne_f32_e32 v48, v48
	v_cvt_i32_f32_sdwa v55, v48 dst_sel:BYTE_3 dst_unused:UNUSED_PAD src0_sel:DWORD
	ds_read2_b32 v[48:49], v57 offset0:8 offset1:41
	v_lshlrev_b32_e32 v56, 8, v56
	v_perm_b32 v53, v56, v53, s0
	v_and_b32_e32 v54, 0xff0000, v54
	v_or3_b32 v53, v53, v54, v55
	ds_read2_b32 v[54:55], v57 offset0:74 offset1:107
	s_waitcnt lgkmcnt(1)
	v_mul_f32_e32 v48, v0, v48
	v_rndne_f32_e32 v48, v48
	v_cvt_i32_f32_e32 v56, v48
	v_mul_f32_e32 v48, v0, v49
	v_rndne_f32_e32 v48, v48
	v_cvt_i32_f32_e32 v59, v48
	s_waitcnt lgkmcnt(0)
	v_mul_f32_e32 v48, v0, v54
	v_rndne_f32_e32 v48, v48
	v_cvt_i32_f32_sdwa v54, v48 dst_sel:WORD_1 dst_unused:UNUSED_PAD src0_sel:DWORD
	v_mul_f32_e32 v48, v0, v55
	v_rndne_f32_e32 v48, v48
	v_cvt_i32_f32_sdwa v55, v48 dst_sel:BYTE_3 dst_unused:UNUSED_PAD src0_sel:DWORD
	ds_read2_b32 v[48:49], v57 offset0:140 offset1:173
	v_lshlrev_b32_e32 v59, 8, v59
	v_perm_b32 v56, v59, v56, s0
	v_and_b32_e32 v54, 0xff0000, v54
	v_or3_b32 v54, v56, v54, v55
	ds_read2_b32 v[56:57], v57 offset0:206 offset1:239
	s_waitcnt lgkmcnt(1)
	v_mul_f32_e32 v48, v0, v48
	v_mul_f32_e32 v49, v0, v49
	v_rndne_f32_e32 v48, v48
	v_rndne_f32_e32 v49, v49
	v_cvt_i32_f32_e32 v55, v48
	s_waitcnt lgkmcnt(0)
	v_mul_f32_e32 v48, v0, v56
	v_cvt_i32_f32_e32 v49, v49
	v_rndne_f32_e32 v48, v48
	v_cvt_i32_f32_sdwa v56, v48 dst_sel:WORD_1 dst_unused:UNUSED_PAD src0_sel:DWORD
	v_mul_f32_e32 v48, v0, v57
	v_rndne_f32_e32 v48, v48
	v_cvt_i32_f32_sdwa v57, v48 dst_sel:BYTE_3 dst_unused:UNUSED_PAD src0_sel:DWORD
	v_lshlrev_b32_e32 v59, 8, v49
	ds_read2_b32 v[48:49], v60 offset0:16 offset1:49
	v_perm_b32 v55, v59, v55, s0
	v_and_b32_e32 v56, 0xff0000, v56
	v_lshl_add_u64 v[46:47], v[46:47], 0, v[2:3]
	v_or3_b32 v55, v55, v56, v57
	global_store_dwordx4 v[46:47], v[52:55], off
	ds_read2_b32 v[52:53], v60 offset0:82 offset1:115
	s_waitcnt lgkmcnt(1)
	v_mul_f32_e32 v48, v0, v48
	v_rndne_f32_e32 v48, v48
	v_cvt_i32_f32_e32 v54, v48
	v_mul_f32_e32 v48, v0, v49
	v_rndne_f32_e32 v48, v48
	v_cvt_i32_f32_e32 v55, v48
	s_waitcnt lgkmcnt(0)
	v_mul_f32_e32 v48, v0, v52
	v_rndne_f32_e32 v48, v48
	v_cvt_i32_f32_sdwa v52, v48 dst_sel:WORD_1 dst_unused:UNUSED_PAD src0_sel:DWORD
	v_mul_f32_e32 v48, v0, v53
	v_rndne_f32_e32 v48, v48
	v_cvt_i32_f32_sdwa v53, v48 dst_sel:BYTE_3 dst_unused:UNUSED_PAD src0_sel:DWORD
	ds_read2_b32 v[48:49], v60 offset0:148 offset1:181
	v_lshlrev_b32_e32 v55, 8, v55
	v_perm_b32 v54, v55, v54, s0
	v_and_b32_e32 v52, 0xff0000, v52
	v_or3_b32 v52, v54, v52, v53
	ds_read2_b32 v[54:55], v60 offset0:214 offset1:247
	s_waitcnt lgkmcnt(1)
	v_mul_f32_e32 v48, v0, v48
	v_rndne_f32_e32 v48, v48
	v_cvt_i32_f32_e32 v53, v48
	v_mul_f32_e32 v48, v0, v49
	v_rndne_f32_e32 v48, v48
	v_cvt_i32_f32_e32 v56, v48
	s_waitcnt lgkmcnt(0)
	v_mul_f32_e32 v48, v0, v54
	v_rndne_f32_e32 v48, v48
	v_cvt_i32_f32_sdwa v54, v48 dst_sel:WORD_1 dst_unused:UNUSED_PAD src0_sel:DWORD
	v_mul_f32_e32 v48, v0, v55
	v_rndne_f32_e32 v48, v48
	v_add_u32_e32 v57, 0xc00, v6
	v_cvt_i32_f32_sdwa v55, v48 dst_sel:BYTE_3 dst_unused:UNUSED_PAD src0_sel:DWORD
	ds_read2_b32 v[48:49], v57 offset0:24 offset1:57
	v_lshlrev_b32_e32 v56, 8, v56
	v_perm_b32 v53, v56, v53, s0
	v_and_b32_e32 v54, 0xff0000, v54
	v_or3_b32 v53, v53, v54, v55
	ds_read2_b32 v[54:55], v57 offset0:90 offset1:123
	s_waitcnt lgkmcnt(1)
	v_mul_f32_e32 v48, v0, v48
	v_rndne_f32_e32 v48, v48
	v_cvt_i32_f32_e32 v56, v48
	v_mul_f32_e32 v48, v0, v49
	v_rndne_f32_e32 v48, v48
	v_cvt_i32_f32_e32 v59, v48
	s_waitcnt lgkmcnt(0)
	v_mul_f32_e32 v48, v0, v54
	v_rndne_f32_e32 v48, v48
	v_cvt_i32_f32_sdwa v54, v48 dst_sel:WORD_1 dst_unused:UNUSED_PAD src0_sel:DWORD
	v_mul_f32_e32 v48, v0, v55
	v_rndne_f32_e32 v48, v48
	v_cvt_i32_f32_sdwa v55, v48 dst_sel:BYTE_3 dst_unused:UNUSED_PAD src0_sel:DWORD
	ds_read2_b32 v[48:49], v57 offset0:156 offset1:189
	v_lshlrev_b32_e32 v59, 8, v59
	v_perm_b32 v56, v59, v56, s0
	v_and_b32_e32 v54, 0xff0000, v54
	v_or3_b32 v54, v56, v54, v55
	ds_read2_b32 v[56:57], v57 offset0:222 offset1:255
	s_waitcnt lgkmcnt(1)
	v_mul_f32_e32 v48, v0, v48
	v_mul_f32_e32 v49, v0, v49
	v_rndne_f32_e32 v48, v48
	v_rndne_f32_e32 v49, v49
	v_cvt_i32_f32_e32 v55, v48
	s_waitcnt lgkmcnt(0)
	v_mul_f32_e32 v48, v0, v56
	v_cvt_i32_f32_e32 v49, v49
	v_rndne_f32_e32 v48, v48
	v_cvt_i32_f32_sdwa v56, v48 dst_sel:WORD_1 dst_unused:UNUSED_PAD src0_sel:DWORD
	v_mul_f32_e32 v48, v0, v57
	v_rndne_f32_e32 v48, v48
	v_cvt_i32_f32_sdwa v57, v48 dst_sel:BYTE_3 dst_unused:UNUSED_PAD src0_sel:DWORD
	v_add_u32_e32 v60, 0x1000, v6
	v_lshlrev_b32_e32 v59, 8, v49
	ds_read2_b32 v[48:49], v60 offset0:32 offset1:65
	v_perm_b32 v55, v59, v55, s0
	v_and_b32_e32 v56, 0xff0000, v56
	v_or3_b32 v55, v55, v56, v57
	global_store_dwordx4 v[46:47], v[52:55], off offset:16
	ds_read2_b32 v[52:53], v60 offset0:98 offset1:131
	s_waitcnt lgkmcnt(1)
	v_mul_f32_e32 v48, v0, v48
	v_rndne_f32_e32 v48, v48
	v_cvt_i32_f32_e32 v54, v48
	v_mul_f32_e32 v48, v0, v49
	v_rndne_f32_e32 v48, v48
	v_cvt_i32_f32_e32 v55, v48
	s_waitcnt lgkmcnt(0)
	v_mul_f32_e32 v48, v0, v52
	v_rndne_f32_e32 v48, v48
	v_cvt_i32_f32_sdwa v52, v48 dst_sel:WORD_1 dst_unused:UNUSED_PAD src0_sel:DWORD
	v_mul_f32_e32 v48, v0, v53
	v_rndne_f32_e32 v48, v48
	v_cvt_i32_f32_sdwa v53, v48 dst_sel:BYTE_3 dst_unused:UNUSED_PAD src0_sel:DWORD
	ds_read2_b32 v[48:49], v60 offset0:164 offset1:197
	v_lshlrev_b32_e32 v55, 8, v55
	v_perm_b32 v54, v55, v54, s0
	v_and_b32_e32 v52, 0xff0000, v52
	v_or3_b32 v52, v54, v52, v53
	v_add_u32_e32 v53, 0x1200, v6
	ds_read2_b32 v[54:55], v53 offset0:102 offset1:135
	s_waitcnt lgkmcnt(1)
	v_mul_f32_e32 v48, v0, v48
	v_rndne_f32_e32 v48, v48
	v_cvt_i32_f32_e32 v53, v48
	v_mul_f32_e32 v48, v0, v49
	v_rndne_f32_e32 v48, v48
	v_cvt_i32_f32_e32 v56, v48
	s_waitcnt lgkmcnt(0)
	v_mul_f32_e32 v48, v0, v54
	v_rndne_f32_e32 v48, v48
	v_cvt_i32_f32_sdwa v54, v48 dst_sel:WORD_1 dst_unused:UNUSED_PAD src0_sel:DWORD
	v_mul_f32_e32 v48, v0, v55
	v_rndne_f32_e32 v48, v48
	v_add_u32_e32 v57, 0x1400, v6
	v_cvt_i32_f32_sdwa v55, v48 dst_sel:BYTE_3 dst_unused:UNUSED_PAD src0_sel:DWORD
	ds_read2_b32 v[48:49], v57 offset0:40 offset1:73
	v_lshlrev_b32_e32 v56, 8, v56
	v_perm_b32 v53, v56, v53, s0
	v_and_b32_e32 v54, 0xff0000, v54
	v_or3_b32 v53, v53, v54, v55
	ds_read2_b32 v[54:55], v57 offset0:106 offset1:139
	s_waitcnt lgkmcnt(1)
	v_mul_f32_e32 v48, v0, v48
	v_rndne_f32_e32 v48, v48
	v_cvt_i32_f32_e32 v56, v48
	v_mul_f32_e32 v48, v0, v49
	v_rndne_f32_e32 v48, v48
	v_cvt_i32_f32_e32 v59, v48
	s_waitcnt lgkmcnt(0)
	v_mul_f32_e32 v48, v0, v54
	v_rndne_f32_e32 v48, v48
	v_cvt_i32_f32_sdwa v54, v48 dst_sel:WORD_1 dst_unused:UNUSED_PAD src0_sel:DWORD
	v_mul_f32_e32 v48, v0, v55
	v_rndne_f32_e32 v48, v48
	v_cvt_i32_f32_sdwa v55, v48 dst_sel:BYTE_3 dst_unused:UNUSED_PAD src0_sel:DWORD
	ds_read2_b32 v[48:49], v57 offset0:172 offset1:205
	v_lshlrev_b32_e32 v57, 8, v59
	v_perm_b32 v56, v57, v56, s0
	v_and_b32_e32 v54, 0xff0000, v54
	v_or3_b32 v54, v56, v54, v55
	v_add_u32_e32 v55, 0x1600, v6
	ds_read2_b32 v[56:57], v55 offset0:110 offset1:143
	s_waitcnt lgkmcnt(1)
	v_mul_f32_e32 v48, v0, v48
	v_mul_f32_e32 v49, v0, v49
	v_rndne_f32_e32 v48, v48
	v_rndne_f32_e32 v49, v49
	v_cvt_i32_f32_e32 v55, v48
	s_waitcnt lgkmcnt(0)
	v_mul_f32_e32 v48, v0, v56
	v_cvt_i32_f32_e32 v49, v49
	v_rndne_f32_e32 v48, v48
	v_cvt_i32_f32_sdwa v56, v48 dst_sel:WORD_1 dst_unused:UNUSED_PAD src0_sel:DWORD
	v_mul_f32_e32 v48, v0, v57
	v_rndne_f32_e32 v48, v48
	v_cvt_i32_f32_sdwa v57, v48 dst_sel:BYTE_3 dst_unused:UNUSED_PAD src0_sel:DWORD
	v_add_u32_e32 v60, 0x1800, v6
	v_lshlrev_b32_e32 v59, 8, v49
	ds_read2_b32 v[48:49], v60 offset0:48 offset1:81
	v_perm_b32 v55, v59, v55, s0
	v_and_b32_e32 v56, 0xff0000, v56
	v_or3_b32 v55, v55, v56, v57
	global_store_dwordx4 v[46:47], v[52:55], off offset:32
	ds_read2_b32 v[52:53], v60 offset0:114 offset1:147
	s_waitcnt lgkmcnt(1)
	v_mul_f32_e32 v48, v0, v48
	v_rndne_f32_e32 v48, v48
	v_cvt_i32_f32_e32 v54, v48
	v_mul_f32_e32 v48, v0, v49
	v_rndne_f32_e32 v48, v48
	v_cvt_i32_f32_e32 v55, v48
	s_waitcnt lgkmcnt(0)
	v_mul_f32_e32 v48, v0, v52
	v_rndne_f32_e32 v48, v48
	v_cvt_i32_f32_sdwa v52, v48 dst_sel:WORD_1 dst_unused:UNUSED_PAD src0_sel:DWORD
	v_mul_f32_e32 v48, v0, v53
	v_rndne_f32_e32 v48, v48
	v_cvt_i32_f32_sdwa v53, v48 dst_sel:BYTE_3 dst_unused:UNUSED_PAD src0_sel:DWORD
	ds_read2_b32 v[48:49], v60 offset0:180 offset1:213
	v_lshlrev_b32_e32 v55, 8, v55
	v_perm_b32 v54, v55, v54, s0
	v_and_b32_e32 v52, 0xff0000, v52
	v_or3_b32 v52, v54, v52, v53
	v_add_u32_e32 v53, 0x1a00, v6
	ds_read2_b32 v[54:55], v53 offset0:118 offset1:151
	s_waitcnt lgkmcnt(1)
	v_mul_f32_e32 v48, v0, v48
	v_rndne_f32_e32 v48, v48
	v_cvt_i32_f32_e32 v53, v48
	v_mul_f32_e32 v48, v0, v49
	v_rndne_f32_e32 v48, v48
	v_cvt_i32_f32_e32 v56, v48
	s_waitcnt lgkmcnt(0)
	v_mul_f32_e32 v48, v0, v54
	v_rndne_f32_e32 v48, v48
	v_cvt_i32_f32_sdwa v54, v48 dst_sel:WORD_1 dst_unused:UNUSED_PAD src0_sel:DWORD
	v_mul_f32_e32 v48, v0, v55
	v_rndne_f32_e32 v48, v48
	v_add_u32_e32 v57, 0x1c00, v6
	v_cvt_i32_f32_sdwa v55, v48 dst_sel:BYTE_3 dst_unused:UNUSED_PAD src0_sel:DWORD
	ds_read2_b32 v[48:49], v57 offset0:56 offset1:89
	v_lshlrev_b32_e32 v56, 8, v56
	v_perm_b32 v53, v56, v53, s0
	v_and_b32_e32 v54, 0xff0000, v54
	v_or3_b32 v53, v53, v54, v55
	ds_read2_b32 v[54:55], v57 offset0:122 offset1:155
	s_waitcnt lgkmcnt(1)
	v_mul_f32_e32 v48, v0, v48
	v_rndne_f32_e32 v48, v48
	v_cvt_i32_f32_e32 v56, v48
	v_mul_f32_e32 v48, v0, v49
	v_rndne_f32_e32 v48, v48
	v_cvt_i32_f32_e32 v59, v48
	s_waitcnt lgkmcnt(0)
	v_mul_f32_e32 v48, v0, v54
	v_rndne_f32_e32 v48, v48
	v_cvt_i32_f32_sdwa v54, v48 dst_sel:WORD_1 dst_unused:UNUSED_PAD src0_sel:DWORD
	v_mul_f32_e32 v48, v0, v55
	v_rndne_f32_e32 v48, v48
	v_cvt_i32_f32_sdwa v55, v48 dst_sel:BYTE_3 dst_unused:UNUSED_PAD src0_sel:DWORD
	ds_read2_b32 v[48:49], v57 offset0:188 offset1:221
	v_mul_f32_e32 v44, v0, v44
	v_rndne_f32_e32 v44, v44
	v_cvt_i32_f32_sdwa v44, v44 dst_sel:WORD_1 dst_unused:UNUSED_PAD src0_sel:DWORD
	v_lshlrev_b32_e32 v57, 8, v59
	s_waitcnt lgkmcnt(0)
	v_mul_f32_e32 v49, v0, v49
	v_mul_f32_e32 v48, v0, v48
	v_rndne_f32_e32 v49, v49
	v_rndne_f32_e32 v48, v48
	v_cvt_i32_f32_e32 v49, v49
	v_cvt_i32_f32_e32 v48, v48
	v_mul_f32_e32 v0, v0, v58
	v_rndne_f32_e32 v0, v0
	v_cvt_i32_f32_sdwa v0, v0 dst_sel:BYTE_3 dst_unused:UNUSED_PAD src0_sel:DWORD
	v_lshlrev_b32_e32 v49, 8, v49
	v_perm_b32 v56, v57, v56, s0
	v_perm_b32 v48, v49, v48, s0
	s_add_i32 s98, s98, s100
	v_and_b32_e32 v54, 0xff0000, v54
	v_and_b32_e32 v44, 0xff0000, v44
	s_mov_b32 s0, 0xfffffc00
	s_cmp_lt_u32 s98, 0x1278
	s_cselect_b32 s0, 0xfffffc00, s0
	s_cmp_lt_u32 s98, 0x11d0
	s_cselect_b32 s0, 0xfffffc00, s0
	s_cmp_lt_u32 s98, 0x10e0
	s_cselect_b32 s0, 0xfffffc00, s0
	s_cmp_lt_u32 s98, 0xf40
	s_cselect_b32 s0, 0xfffffc00, s0
	s_cmp_lt_u32 s98, 0xc60
	s_cselect_b32 s0, 0x700, s0
	s_cmp_lt_u32 s98, 0xc40
	s_cselect_b32 s0, 0x6a0, s0
	s_cmp_lt_u32 s98, 0xc00
	s_cselect_b32 s0, 0x6a0, s0
	s_cmp_lt_u32 s98, 0xb60
	s_cselect_b32 s0, 0xfffff600, s0
	s_cmp_lt_u32 s98, 0xab0
	s_cselect_b32 s0, 0x890, s0
	s_cmp_lt_u32 s98, 0xa90
	s_cselect_b32 s0, 0x770, s0
	s_cmp_lt_u32 s98, 0xa20
	s_cselect_b32 s0, 0x770, s0
	s_cmp_lt_u32 s98, 0x9b0
	s_cselect_b32 s0, 0xfffffeb0, s0
	s_cmp_lt_u32 s98, 0x880
	s_cselect_b32 s0, 0xfffffeb0, s0
	s_cmp_lt_u32 s98, 0x5b0
	s_cselect_b32 s0, 0xfffffeb0, s0
	s_cmp_lt_u32 s98, 0x460
	s_cselect_b32 s0, 0xfffffeb0, s0
	s_cmp_lt_u32 s98, 0x2b0
	s_cselect_b32 s0, 0x1070, s0
	s_cmp_lt_u32 s98, 0x290
	s_cselect_b32 s0, 0xe90, s0
	s_cmp_lt_u32 s98, 0x280
	s_cselect_b32 s0, 0xe90, s0
	s_cmp_lt_u32 s98, 0x1b0
	s_cselect_b32 s0, 0xffffff00, s0
	s_cmp_lt_u32 s98, 0x100
	s_cselect_b32 s0, 0x1200, s0
	s_cmp_lt_u32 s98, 0xe0
	s_cselect_b32 s0, 0xf60, s0
	s_add_i32 s28, s98, s0
	v_or3_b32 v54, v56, v54, v55
	v_or3_b32 v55, v48, v44, v0
	s_cmp_ge_u32 s98, s99
	global_store_dwordx4 v[46:47], v[52:55], off offset:48
	s_barrier
	s_cbranch_scc1 .Lwqd_exit

.Lwqd_exit:
	s_mov_b64 exec, -1
	s_cmp_eq_u32 s101, 1
	s_cbranch_scc1 .Lwqd_ret_A
	s_cmp_eq_u32 s101, 2
	s_cbranch_scc1 .Lwqd_ret_F
	s_cmp_eq_u32 s101, 3
	s_cbranch_scc1 .Lwqd_ret_M
	s_cmp_eq_u32 s101, 4
	s_cbranch_scc1 .Lwqd_ret_G
	s_cmp_eq_u32 s101, 5
	s_cbranch_scc1 .Lwqd_ret_H
	s_endpgm

.LBB0_1159:
	v_readlane_b32 s98, v251, 3
	v_readlane_b32 s99, v255, 29
	s_cmp_lt_u32 s98, 16
	s_cbranch_scc1 .Lwqd_skip_A
	s_sub_i32 s98, s98, 16
	s_mov_b32 s100, 0
	s_mov_b32 s101, 0
	s_cmp_eq_u32 s99, 0
	s_cselect_b32 s100, 0x280, s100
	s_cselect_b32 s101, 0x460, s101
	s_cmp_eq_u32 s99, 1
	s_cselect_b32 s100, 0xa20, s100
	s_cselect_b32 s101, 0xc00, s101
	s_cmp_eq_u32 s99, 2
	s_cselect_b32 s100, 0x10e0, s100
	s_cselect_b32 s101, 0x11d0, s101
	s_add_i32 s98, s98, s100
	s_mov_b32 s99, s101
	s_cmp_ge_u32 s98, s99
	s_cbranch_scc1 .Lwqd_skip_A
	s_movk_i32 s100, 240
	s_mov_b32 s101, 1
	v_writelane_b32 v117, s0, 0
	v_writelane_b32 v117, s1, 1
	v_writelane_b32 v117, s2, 2
	v_writelane_b32 v117, s3, 3
	v_writelane_b32 v117, s4, 4
	v_writelane_b32 v117, s5, 5
	v_writelane_b32 v117, s6, 6
	v_writelane_b32 v117, s7, 7
	v_writelane_b32 v117, s8, 8
	v_writelane_b32 v117, s9, 9
	v_writelane_b32 v117, s10, 10
	v_writelane_b32 v117, s11, 11
	v_writelane_b32 v117, s12, 12
	v_writelane_b32 v117, s13, 13
	v_writelane_b32 v117, s14, 14
	v_writelane_b32 v117, s15, 15
	v_writelane_b32 v117, s16, 16
	v_writelane_b32 v117, s17, 17
	v_writelane_b32 v117, s18, 18
	v_writelane_b32 v117, s19, 19
	v_writelane_b32 v117, s20, 20
	v_writelane_b32 v117, s21, 21
	v_writelane_b32 v117, s22, 22
	v_writelane_b32 v117, s23, 23
	v_writelane_b32 v117, s24, 24
	v_writelane_b32 v117, s25, 25
	v_writelane_b32 v117, s26, 26
	v_writelane_b32 v117, s27, 27
	v_writelane_b32 v117, s28, 28
	v_writelane_b32 v117, s29, 29
	v_writelane_b32 v117, s30, 30
	v_writelane_b32 v117, s31, 31
	v_writelane_b32 v117, s32, 32
	v_writelane_b32 v117, s33, 33
	v_writelane_b32 v117, s34, 34
	v_writelane_b32 v117, s35, 35
	v_writelane_b32 v117, s36, 36
	v_writelane_b32 v117, s37, 37
	v_writelane_b32 v117, s38, 38
	v_writelane_b32 v117, s39, 39
	v_writelane_b32 v117, s40, 40
	v_writelane_b32 v117, s41, 41
	v_writelane_b32 v117, s42, 42
	v_writelane_b32 v117, s43, 43
	v_writelane_b32 v117, s44, 44
	v_writelane_b32 v117, s45, 45
	v_writelane_b32 v117, s46, 46
	v_writelane_b32 v117, s47, 47
	v_writelane_b32 v117, s48, 48
	v_writelane_b32 v117, s49, 49
	v_writelane_b32 v117, s50, 50
	v_writelane_b32 v117, s51, 51
	v_writelane_b32 v117, s52, 52
	v_writelane_b32 v117, s53, 53
	v_writelane_b32 v117, s54, 54
	v_writelane_b32 v117, s55, 55
	v_writelane_b32 v117, s56, 56
	v_writelane_b32 v117, s57, 57
	v_writelane_b32 v117, s58, 58
	v_writelane_b32 v117, s59, 59
	v_writelane_b32 v117, s60, 60
	v_writelane_b32 v117, s61, 61
	v_writelane_b32 v117, s62, 62
	v_writelane_b32 v117, s63, 63
	v_writelane_b32 v118, s64, 0
	v_writelane_b32 v118, s65, 1
	v_writelane_b32 v118, s66, 2
	v_writelane_b32 v118, s67, 3
	v_writelane_b32 v118, s68, 4
	v_writelane_b32 v118, s69, 5
	v_writelane_b32 v118, s70, 6
	v_writelane_b32 v118, s71, 7
	v_writelane_b32 v118, s72, 8
	v_writelane_b32 v118, s73, 9
	v_writelane_b32 v118, s74, 10
	v_writelane_b32 v118, s75, 11
	v_writelane_b32 v118, s76, 12
	v_writelane_b32 v118, s77, 13
	v_writelane_b32 v118, s78, 14
	v_writelane_b32 v118, s79, 15
	v_writelane_b32 v118, s80, 16
	v_writelane_b32 v118, s81, 17
	v_writelane_b32 v118, s82, 18
	v_writelane_b32 v118, s83, 19
	v_writelane_b32 v118, s84, 20
	v_writelane_b32 v118, s85, 21
	v_writelane_b32 v118, s86, 22
	v_writelane_b32 v118, s87, 23
	v_writelane_b32 v118, s88, 24
	v_writelane_b32 v118, s89, 25
	v_writelane_b32 v118, s90, 26
	v_writelane_b32 v118, s91, 27
	v_writelane_b32 v118, s92, 28
	v_writelane_b32 v118, s93, 29
	v_writelane_b32 v118, s94, 30
	v_writelane_b32 v118, s95, 31
	v_writelane_b32 v118, s96, 32
	v_writelane_b32 v118, s97, 33
	v_mov_b32_e32 v100, v0
	v_mov_b32_e32 v101, v50
	v_mov_b32_e32 v102, v51
	v_mov_b32_e32 v103, v52
	v_mov_b32_e32 v104, v54
	v_mov_b32_e32 v105, v55
	v_mov_b32_e32 v106, v56
	v_mov_b32_e32 v107, v58
	v_mov_b32_e32 v108, v59
	v_mov_b32_e32 v109, v60
	v_mov_b32_e32 v110, v62
	v_mov_b32_e32 v111, v63
	v_mov_b32_e32 v112, v64
	v_mov_b32_e32 v113, v67
	v_mov_b32_e32 v114, v75
	v_mov_b32_e32 v115, v77
	s_branch .Lwqd_entry

.LBB0_1542:
	s_or_b64 exec, exec, s[0:1]
	v_readlane_b32 s36, v251, 5
	v_readlane_b32 s42, v251, 11
	v_readlane_b32 s43, v251, 12
	s_mov_b64 s[0:1], s[42:43]
	v_mov_b32_e32 v1, v246
	s_mov_b32 s100, s95
	s_lshl_b32 s2, s95, 2
	v_readlane_b32 s3, v251, 3
	s_waitcnt lgkmcnt(0)
	s_barrier
	s_cmp_lt_i32 s3, s2
	v_readfirstlane_b32 s8, v1
	v_readlane_b32 s37, v251, 6
	v_readlane_b32 s38, v251, 7
	v_readlane_b32 s39, v251, 8
	v_readlane_b32 s40, v251, 9
	v_readlane_b32 s41, v251, 10
	s_cbranch_scc0 .LBB0_1570
	s_lshr_b32 s3, s95, 31
	s_add_i32 s3, s95, s3
	s_ashr_i32 s5, s3, 1
	s_ashr_i32 s3, s2, 31
	s_lshr_b32 s4, s3, 29
	s_add_i32 s4, s2, s4
	s_and_b32 s4, s4, -8
	s_sub_i32 s10, s2, s4
	v_writelane_b32 v255, s5, 35
	s_add_i32 s11, s5, 1
	v_readlane_b32 s4, v254, 56
	v_writelane_b32 v255, s11, 37
	s_mul_i32 s11, s11, s10
	s_cmp_ge_i32 s4, s10
	s_mov_b64 s[4:5], -1
	v_writelane_b32 v255, s11, 38
	s_cbranch_scc0 .LBB0_1545
	v_readlane_b32 s4, v254, 56
	s_sub_i32 s4, s4, s10
	v_readlane_b32 s5, v255, 35
	s_mul_i32 s4, s4, s5
	v_readlane_b32 s5, v255, 38
	s_add_i32 s14, s4, s5
	s_mov_b64 s[4:5], 0

.LBB0_1570:
	v_readlane_b32 s99, v255, 29
	s_cmp_eq_u32 s99, 1
	s_cbranch_scc0 .Lwqd_skip_H
	s_lshl_b32 s101, s100, 2
	s_and_b32 s101, s101, 0xff
	v_readlane_b32 s98, v251, 3
	s_cmp_lt_u32 s98, s101
	s_cbranch_scc1 .Lwqd_skip_H
	s_sub_i32 s98, s98, s101
	s_sub_i32 s100, 0x100, s101
	s_add_i32 s98, s98, 0xc00
	s_mov_b32 s99, 0xf40
	s_cmp_ge_u32 s98, s99
	s_cbranch_scc1 .Lwqd_skip_H
	s_mov_b32 s101, 5
	v_writelane_b32 v117, s0, 0
	v_writelane_b32 v117, s1, 1
	v_writelane_b32 v117, s2, 2
	v_writelane_b32 v117, s3, 3
	v_writelane_b32 v117, s4, 4
	v_writelane_b32 v117, s5, 5
	v_writelane_b32 v117, s6, 6
	v_writelane_b32 v117, s7, 7
	v_writelane_b32 v117, s8, 8
	v_writelane_b32 v117, s9, 9
	v_writelane_b32 v117, s10, 10
	v_writelane_b32 v117, s11, 11
	v_writelane_b32 v117, s12, 12
	v_writelane_b32 v117, s13, 13
	v_writelane_b32 v117, s14, 14
	v_writelane_b32 v117, s15, 15
	v_writelane_b32 v117, s16, 16
	v_writelane_b32 v117, s17, 17
	v_writelane_b32 v117, s18, 18
	v_writelane_b32 v117, s19, 19
	v_writelane_b32 v117, s20, 20
	v_writelane_b32 v117, s21, 21
	v_writelane_b32 v117, s22, 22
	v_writelane_b32 v117, s23, 23
	v_writelane_b32 v117, s24, 24
	v_writelane_b32 v117, s25, 25
	v_writelane_b32 v117, s26, 26
	v_writelane_b32 v117, s27, 27
	v_writelane_b32 v117, s28, 28
	v_writelane_b32 v117, s29, 29
	v_writelane_b32 v117, s30, 30
	v_writelane_b32 v117, s31, 31
	v_writelane_b32 v117, s32, 32
	v_writelane_b32 v117, s33, 33
	v_writelane_b32 v117, s34, 34
	v_writelane_b32 v117, s35, 35
	v_writelane_b32 v117, s36, 36
	v_writelane_b32 v117, s37, 37
	v_writelane_b32 v117, s38, 38
	v_writelane_b32 v117, s39, 39
	v_writelane_b32 v117, s40, 40
	v_writelane_b32 v117, s41, 41
	v_writelane_b32 v117, s42, 42
	v_writelane_b32 v117, s43, 43
	v_writelane_b32 v117, s44, 44
	v_writelane_b32 v117, s45, 45
	v_writelane_b32 v117, s46, 46
	v_writelane_b32 v117, s47, 47
	v_writelane_b32 v117, s48, 48
	v_writelane_b32 v117, s49, 49
	v_writelane_b32 v117, s50, 50
	v_writelane_b32 v117, s51, 51
	v_writelane_b32 v117, s52, 52
	v_writelane_b32 v117, s53, 53
	v_writelane_b32 v117, s54, 54
	v_writelane_b32 v117, s55, 55
	v_writelane_b32 v117, s56, 56
	v_writelane_b32 v117, s57, 57
	v_writelane_b32 v117, s58, 58
	v_writelane_b32 v117, s59, 59
	v_writelane_b32 v117, s60, 60
	v_writelane_b32 v117, s61, 61
	v_writelane_b32 v117, s62, 62
	v_writelane_b32 v117, s63, 63
	v_writelane_b32 v118, s64, 0
	v_writelane_b32 v118, s65, 1
	v_writelane_b32 v118, s66, 2
	v_writelane_b32 v118, s67, 3
	v_writelane_b32 v118, s68, 4
	v_writelane_b32 v118, s69, 5
	v_writelane_b32 v118, s70, 6
	v_writelane_b32 v118, s71, 7
	v_writelane_b32 v118, s72, 8
	v_writelane_b32 v118, s73, 9
	v_writelane_b32 v118, s74, 10
	v_writelane_b32 v118, s75, 11
	v_writelane_b32 v118, s76, 12
	v_writelane_b32 v118, s77, 13
	v_writelane_b32 v118, s78, 14
	v_writelane_b32 v118, s79, 15
	v_writelane_b32 v118, s80, 16
	v_writelane_b32 v118, s81, 17
	v_writelane_b32 v118, s82, 18
	v_writelane_b32 v118, s83, 19
	v_writelane_b32 v118, s84, 20
	v_writelane_b32 v118, s85, 21
	v_writelane_b32 v118, s86, 22
	v_writelane_b32 v118, s87, 23
	v_writelane_b32 v118, s88, 24
	v_writelane_b32 v118, s89, 25
	v_writelane_b32 v118, s90, 26
	v_writelane_b32 v118, s91, 27
	v_writelane_b32 v118, s92, 28
	v_writelane_b32 v118, s93, 29
	v_writelane_b32 v118, s94, 30
	v_writelane_b32 v118, s95, 31
	v_writelane_b32 v118, s96, 32
	v_writelane_b32 v118, s97, 33
	v_mov_b32_e32 v100, v0
	v_mov_b32_e32 v101, v50
	v_mov_b32_e32 v102, v51
	v_mov_b32_e32 v103, v52
	v_mov_b32_e32 v104, v54
	v_mov_b32_e32 v105, v55
	v_mov_b32_e32 v106, v56
	v_mov_b32_e32 v107, v58
	v_mov_b32_e32 v108, v59
	v_mov_b32_e32 v109, v60
	v_mov_b32_e32 v110, v62
	v_mov_b32_e32 v111, v63
	v_mov_b32_e32 v112, v64
	v_mov_b32_e32 v113, v67
	v_mov_b32_e32 v114, v75
	v_mov_b32_e32 v115, v77
	s_branch .Lwqd_entry

.LBB0_1699:
	v_readlane_b32 s98, v251, 3
	v_readlane_b32 s99, v255, 29
	s_cmp_lt_u32 s98, 88
	s_cbranch_scc1 .Lwqd_skip_G
	s_sub_i32 s98, s98, 88
	s_mov_b32 s100, 0
	s_mov_b32 s101, 0
	s_cmp_eq_u32 s99, 0
	s_cselect_b32 s100, 0x460, s100
	s_cselect_b32 s101, 0x5b0, s101
	s_cmp_eq_u32 s99, 2
	s_cselect_b32 s100, 0x11d0, s100
	s_cselect_b32 s101, 0x1278, s101
	s_add_i32 s98, s98, s100
	s_mov_b32 s99, s101
	s_cmp_ge_u32 s98, s99
	s_cbranch_scc1 .Lwqd_skip_G
	s_movk_i32 s100, 168
	s_mov_b32 s101, 4
	v_writelane_b32 v117, s0, 0
	v_writelane_b32 v117, s1, 1
	v_writelane_b32 v117, s2, 2
	v_writelane_b32 v117, s3, 3
	v_writelane_b32 v117, s4, 4
	v_writelane_b32 v117, s5, 5
	v_writelane_b32 v117, s6, 6
	v_writelane_b32 v117, s7, 7
	v_writelane_b32 v117, s8, 8
	v_writelane_b32 v117, s9, 9
	v_writelane_b32 v117, s10, 10
	v_writelane_b32 v117, s11, 11
	v_writelane_b32 v117, s12, 12
	v_writelane_b32 v117, s13, 13
	v_writelane_b32 v117, s14, 14
	v_writelane_b32 v117, s15, 15
	v_writelane_b32 v117, s16, 16
	v_writelane_b32 v117, s17, 17
	v_writelane_b32 v117, s18, 18
	v_writelane_b32 v117, s19, 19
	v_writelane_b32 v117, s20, 20
	v_writelane_b32 v117, s21, 21
	v_writelane_b32 v117, s22, 22
	v_writelane_b32 v117, s23, 23
	v_writelane_b32 v117, s24, 24
	v_writelane_b32 v117, s25, 25
	v_writelane_b32 v117, s26, 26
	v_writelane_b32 v117, s27, 27
	v_writelane_b32 v117, s28, 28
	v_writelane_b32 v117, s29, 29
	v_writelane_b32 v117, s30, 30
	v_writelane_b32 v117, s31, 31
	v_writelane_b32 v117, s32, 32
	v_writelane_b32 v117, s33, 33
	v_writelane_b32 v117, s34, 34
	v_writelane_b32 v117, s35, 35
	v_writelane_b32 v117, s36, 36
	v_writelane_b32 v117, s37, 37
	v_writelane_b32 v117, s38, 38
	v_writelane_b32 v117, s39, 39
	v_writelane_b32 v117, s40, 40
	v_writelane_b32 v117, s41, 41
	v_writelane_b32 v117, s42, 42
	v_writelane_b32 v117, s43, 43
	v_writelane_b32 v117, s44, 44
	v_writelane_b32 v117, s45, 45
	v_writelane_b32 v117, s46, 46
	v_writelane_b32 v117, s47, 47
	v_writelane_b32 v117, s48, 48
	v_writelane_b32 v117, s49, 49
	v_writelane_b32 v117, s50, 50
	v_writelane_b32 v117, s51, 51
	v_writelane_b32 v117, s52, 52
	v_writelane_b32 v117, s53, 53
	v_writelane_b32 v117, s54, 54
	v_writelane_b32 v117, s55, 55
	v_writelane_b32 v117, s56, 56
	v_writelane_b32 v117, s57, 57
	v_writelane_b32 v117, s58, 58
	v_writelane_b32 v117, s59, 59
	v_writelane_b32 v117, s60, 60
	v_writelane_b32 v117, s61, 61
	v_writelane_b32 v117, s62, 62
	v_writelane_b32 v117, s63, 63
	v_writelane_b32 v118, s64, 0
	v_writelane_b32 v118, s65, 1
	v_writelane_b32 v118, s66, 2
	v_writelane_b32 v118, s67, 3
	v_writelane_b32 v118, s68, 4
	v_writelane_b32 v118, s69, 5
	v_writelane_b32 v118, s70, 6
	v_writelane_b32 v118, s71, 7
	v_writelane_b32 v118, s72, 8
	v_writelane_b32 v118, s73, 9
	v_writelane_b32 v118, s74, 10
	v_writelane_b32 v118, s75, 11
	v_writelane_b32 v118, s76, 12
	v_writelane_b32 v118, s77, 13
	v_writelane_b32 v118, s78, 14
	v_writelane_b32 v118, s79, 15
	v_writelane_b32 v118, s80, 16
	v_writelane_b32 v118, s81, 17
	v_writelane_b32 v118, s82, 18
	v_writelane_b32 v118, s83, 19
	v_writelane_b32 v118, s84, 20
	v_writelane_b32 v118, s85, 21
	v_writelane_b32 v118, s86, 22
	v_writelane_b32 v118, s87, 23
	v_writelane_b32 v118, s88, 24
	v_writelane_b32 v118, s89, 25
	v_writelane_b32 v118, s90, 26
	v_writelane_b32 v118, s91, 27
	v_writelane_b32 v118, s92, 28
	v_writelane_b32 v118, s93, 29
	v_writelane_b32 v118, s94, 30
	v_writelane_b32 v118, s95, 31
	v_writelane_b32 v118, s96, 32
	v_writelane_b32 v118, s97, 33
	v_mov_b32_e32 v100, v0
	v_mov_b32_e32 v101, v50
	v_mov_b32_e32 v102, v51
	v_mov_b32_e32 v103, v52
	v_mov_b32_e32 v104, v54
	v_mov_b32_e32 v105, v55
	v_mov_b32_e32 v106, v56
	v_mov_b32_e32 v107, v58
	v_mov_b32_e32 v108, v59
	v_mov_b32_e32 v109, v60
	v_mov_b32_e32 v110, v62
	v_mov_b32_e32 v111, v63
	v_mov_b32_e32 v112, v64
	v_mov_b32_e32 v113, v67
	v_mov_b32_e32 v114, v75
	v_mov_b32_e32 v115, v77
	s_branch .Lwqd_entry

.LBB0_1774:
	v_readlane_b32 s98, v251, 3
	v_readlane_b32 s99, v255, 29
	s_cmp_lt_u32 s98, 16
	s_cbranch_scc1 .Lwqd_skip_F
	s_sub_i32 s98, s98, 16
	s_mov_b32 s100, 0
	s_mov_b32 s101, 0
	s_cmp_eq_u32 s99, 0
	s_cselect_b32 s100, 0x5b0, s100
	s_cselect_b32 s101, 0x880, s101
	s_cmp_eq_u32 s99, 2
	s_cselect_b32 s100, 0x1278, s100
	s_cselect_b32 s101, 0x1360, s101
	s_add_i32 s98, s98, s100
	s_mov_b32 s99, s101
	s_cmp_ge_u32 s98, s99
	s_cbranch_scc1 .Lwqd_skip_F
	s_movk_i32 s100, 240
	s_mov_b32 s101, 2
	v_writelane_b32 v117, s0, 0
	v_writelane_b32 v117, s1, 1
	v_writelane_b32 v117, s2, 2
	v_writelane_b32 v117, s3, 3
	v_writelane_b32 v117, s4, 4
	v_writelane_b32 v117, s5, 5
	v_writelane_b32 v117, s6, 6
	v_writelane_b32 v117, s7, 7
	v_writelane_b32 v117, s8, 8
	v_writelane_b32 v117, s9, 9
	v_writelane_b32 v117, s10, 10
	v_writelane_b32 v117, s11, 11
	v_writelane_b32 v117, s12, 12
	v_writelane_b32 v117, s13, 13
	v_writelane_b32 v117, s14, 14
	v_writelane_b32 v117, s15, 15
	v_writelane_b32 v117, s16, 16
	v_writelane_b32 v117, s17, 17
	v_writelane_b32 v117, s18, 18
	v_writelane_b32 v117, s19, 19
	v_writelane_b32 v117, s20, 20
	v_writelane_b32 v117, s21, 21
	v_writelane_b32 v117, s22, 22
	v_writelane_b32 v117, s23, 23
	v_writelane_b32 v117, s24, 24
	v_writelane_b32 v117, s25, 25
	v_writelane_b32 v117, s26, 26
	v_writelane_b32 v117, s27, 27
	v_writelane_b32 v117, s28, 28
	v_writelane_b32 v117, s29, 29
	v_writelane_b32 v117, s30, 30
	v_writelane_b32 v117, s31, 31
	v_writelane_b32 v117, s32, 32
	v_writelane_b32 v117, s33, 33
	v_writelane_b32 v117, s34, 34
	v_writelane_b32 v117, s35, 35
	v_writelane_b32 v117, s36, 36
	v_writelane_b32 v117, s37, 37
	v_writelane_b32 v117, s38, 38
	v_writelane_b32 v117, s39, 39
	v_writelane_b32 v117, s40, 40
	v_writelane_b32 v117, s41, 41
	v_writelane_b32 v117, s42, 42
	v_writelane_b32 v117, s43, 43
	v_writelane_b32 v117, s44, 44
	v_writelane_b32 v117, s45, 45
	v_writelane_b32 v117, s46, 46
	v_writelane_b32 v117, s47, 47
	v_writelane_b32 v117, s48, 48
	v_writelane_b32 v117, s49, 49
	v_writelane_b32 v117, s50, 50
	v_writelane_b32 v117, s51, 51
	v_writelane_b32 v117, s52, 52
	v_writelane_b32 v117, s53, 53
	v_writelane_b32 v117, s54, 54
	v_writelane_b32 v117, s55, 55
	v_writelane_b32 v117, s56, 56
	v_writelane_b32 v117, s57, 57
	v_writelane_b32 v117, s58, 58
	v_writelane_b32 v117, s59, 59
	v_writelane_b32 v117, s60, 60
	v_writelane_b32 v117, s61, 61
	v_writelane_b32 v117, s62, 62
	v_writelane_b32 v117, s63, 63
	v_writelane_b32 v118, s64, 0
	v_writelane_b32 v118, s65, 1
	v_writelane_b32 v118, s66, 2
	v_writelane_b32 v118, s67, 3
	v_writelane_b32 v118, s68, 4
	v_writelane_b32 v118, s69, 5
	v_writelane_b32 v118, s70, 6
	v_writelane_b32 v118, s71, 7
	v_writelane_b32 v118, s72, 8
	v_writelane_b32 v118, s73, 9
	v_writelane_b32 v118, s74, 10
	v_writelane_b32 v118, s75, 11
	v_writelane_b32 v118, s76, 12
	v_writelane_b32 v118, s77, 13
	v_writelane_b32 v118, s78, 14
	v_writelane_b32 v118, s79, 15
	v_writelane_b32 v118, s80, 16
	v_writelane_b32 v118, s81, 17
	v_writelane_b32 v118, s82, 18
	v_writelane_b32 v118, s83, 19
	v_writelane_b32 v118, s84, 20
	v_writelane_b32 v118, s85, 21
	v_writelane_b32 v118, s86, 22
	v_writelane_b32 v118, s87, 23
	v_writelane_b32 v118, s88, 24
	v_writelane_b32 v118, s89, 25
	v_writelane_b32 v118, s90, 26
	v_writelane_b32 v118, s91, 27
	v_writelane_b32 v118, s92, 28
	v_writelane_b32 v118, s93, 29
	v_writelane_b32 v118, s94, 30
	v_writelane_b32 v118, s95, 31
	v_writelane_b32 v118, s96, 32
	v_writelane_b32 v118, s97, 33
	v_mov_b32_e32 v100, v0
	v_mov_b32_e32 v101, v50
	v_mov_b32_e32 v102, v51
	v_mov_b32_e32 v103, v52
	v_mov_b32_e32 v104, v54
	v_mov_b32_e32 v105, v55
	v_mov_b32_e32 v106, v56
	v_mov_b32_e32 v107, v58
	v_mov_b32_e32 v108, v59
	v_mov_b32_e32 v109, v60
	v_mov_b32_e32 v110, v62
	v_mov_b32_e32 v111, v63
	v_mov_b32_e32 v112, v64
	v_mov_b32_e32 v113, v67
	v_mov_b32_e32 v114, v75
	v_mov_b32_e32 v115, v77
	s_branch .Lwqd_entry
